# grid barrier: the acquiring L1 invalidate (buffer_inv sc1) is issued at arrival (leader: together with its L2 writeback) instead of after the release, so its latency hides behind the wait; no L1-alloc
# speedup vs baseline: 1.0087x; 1.0019x over previous
.LBB0_41:
	s_or_b64 exec, exec, s[14:15]
	v_cvt_f32_u32_e32 v5, v3
	s_waitcnt vmcnt(0)
	v_readfirstlane_b32 s0, v4
	v_sub_u32_e32 v4, 0, v3
	v_rcp_iflag_f32_e32 v5, v5
	v_add_u32_e32 v6, s0, v2
	v_mul_f32_e32 v5, 0x4f7ffffe, v5
	v_cvt_u32_f32_e32 v5, v5
	v_mul_lo_u32 v2, v4, v5
	v_mul_hi_u32 v2, v5, v2
	v_add_u32_e32 v2, v5, v2
	v_mul_hi_u32 v2, v6, v2
	v_mul_lo_u32 v4, v2, v3
	v_sub_u32_e32 v4, v6, v4
	v_add_u32_e32 v5, 1, v2
	v_cmp_ge_u32_e32 vcc, v4, v3
	s_nop 1
	v_cndmask_b32_e32 v2, v2, v5, vcc
	v_sub_u32_e32 v5, v4, v3
	v_cndmask_b32_e32 v4, v4, v5, vcc
	v_add_u32_e32 v5, 1, v2
	v_cmp_ge_u32_e32 vcc, v4, v3
	v_add_u32_e32 v4, 1, v6
	s_nop 0
	v_cndmask_b32_e32 v2, v2, v5, vcc
	v_mul_lo_u32 v5, v3, v2
	v_add_u32_e32 v3, v5, v3
	v_cmp_ne_u32_e32 vcc, v4, v3
	s_and_saveexec_b64 s[0:1], vcc
	s_xor_b64 s[12:13], exec, s[0:1]
	s_cbranch_execz .LBB0_55
	buffer_inv sc1
	s_waitcnt lgkmcnt(0)
	v_mov_b32_e32 v1, 0x2000
	global_load_dword v1, v1, s[10:11] offset:1024 sc1
	s_add_u32 s16, s10, 0x2400
	s_addc_u32 s17, s11, 0
	s_waitcnt vmcnt(0)
	v_cmp_eq_u32_e32 vcc, v1, v2
	s_and_saveexec_b64 s[14:15], vcc
	s_cbranch_execz .LBB0_54
	s_mov_b32 s0, 1
	s_mov_b64 s[18:19], 0
	v_mov_b32_e32 v1, 0
	s_branch .LBB0_45

.LBB0_54:
	s_or_b64 exec, exec, s[14:15]
	s_waitcnt vmcnt(0)
	s_waitcnt vmcnt(0)
.LBB0_55:
	s_andn2_saveexec_b64 s[0:1], s[12:13]
	s_cbranch_execz .LBB0_75
	s_mov_b64 s[12:13], exec
	buffer_wbl2 sc1
	buffer_inv sc1
	s_waitcnt lgkmcnt(0)
	s_waitcnt vmcnt(0)
	v_mbcnt_lo_u32_b32 v2, s12, 0
	v_mbcnt_hi_u32_b32 v2, s13, v2
	v_cmp_eq_u32_e32 vcc, 0, v2
	s_and_saveexec_b64 s[14:15], vcc
	s_cbranch_execz .LBB0_58
	s_bcnt1_i32_b64 s0, s[12:13]
	v_mov_b32_e32 v3, 0x3000
	v_mov_b32_e32 v4, s0
	global_atomic_add v3, v3, v4, s[8:9] offset:1024 sc0

.LBB0_72:
	s_or_b64 exec, exec, s[8:9]
	s_mov_b64 s[8:9], exec
	v_mbcnt_lo_u32_b32 v1, s8, 0
	v_mbcnt_hi_u32_b32 v1, s9, v1
	v_cmp_eq_u32_e32 vcc, 0, v1
	s_waitcnt vmcnt(0)
	s_and_saveexec_b64 s[12:13], vcc
	s_cbranch_execz .LBB0_74
	s_bcnt1_i32_b64 s0, s[8:9]
	v_mov_b32_e32 v1, 0x2000
	v_mov_b32_e32 v2, s0
	global_atomic_add v1, v2, s[10:11] offset:1024

.LBB0_1341:
	s_or_b64 exec, exec, s[16:17]
	v_cvt_f32_u32_e32 v5, v3
	s_waitcnt vmcnt(0)
	v_readfirstlane_b32 s0, v4
	v_sub_u32_e32 v4, 0, v3
	v_rcp_iflag_f32_e32 v5, v5
	v_add_u32_e32 v6, s0, v2
	v_mul_f32_e32 v5, 0x4f7ffffe, v5
	v_cvt_u32_f32_e32 v5, v5
	v_mul_lo_u32 v2, v4, v5
	v_mul_hi_u32 v2, v5, v2
	v_add_u32_e32 v2, v5, v2
	v_mul_hi_u32 v2, v6, v2
	v_mul_lo_u32 v4, v2, v3
	v_sub_u32_e32 v4, v6, v4
	v_add_u32_e32 v5, 1, v2
	v_cmp_ge_u32_e32 vcc, v4, v3
	s_nop 1
	v_cndmask_b32_e32 v2, v2, v5, vcc
	v_sub_u32_e32 v5, v4, v3
	v_cndmask_b32_e32 v4, v4, v5, vcc
	v_add_u32_e32 v5, 1, v2
	v_cmp_ge_u32_e32 vcc, v4, v3
	v_add_u32_e32 v4, 1, v6
	s_nop 0
	v_cndmask_b32_e32 v2, v2, v5, vcc
	v_mul_lo_u32 v5, v3, v2
	v_add_u32_e32 v3, v5, v3
	v_cmp_ne_u32_e32 vcc, v4, v3
	s_and_saveexec_b64 s[0:1], vcc
	s_xor_b64 s[14:15], exec, s[0:1]
	s_cbranch_execz .LBB0_1355
	buffer_inv sc1
	s_waitcnt lgkmcnt(0)
	v_mov_b32_e32 v1, 0x2000
	global_load_dword v1, v1, s[12:13] offset:1024 sc1
	s_add_u32 s18, s12, 0x2400
	s_addc_u32 s19, s13, 0
	s_waitcnt vmcnt(0)
	v_cmp_eq_u32_e32 vcc, v1, v2
	s_and_saveexec_b64 s[16:17], vcc
	s_cbranch_execz .LBB0_1354
	s_mov_b32 s0, 1
	s_mov_b64 s[20:21], 0
	v_mov_b32_e32 v1, 0
	s_branch .LBB0_1345

.LBB0_1354:
	s_or_b64 exec, exec, s[16:17]
	s_waitcnt vmcnt(0)
	s_waitcnt vmcnt(0)
.LBB0_1355:
	s_andn2_saveexec_b64 s[0:1], s[14:15]
	s_cbranch_execz .LBB0_1375
	s_mov_b64 s[14:15], exec
	buffer_wbl2 sc1
	buffer_inv sc1
	s_waitcnt lgkmcnt(0)
	s_waitcnt vmcnt(0)
	v_mbcnt_lo_u32_b32 v2, s14, 0
	v_mbcnt_hi_u32_b32 v2, s15, v2
	v_cmp_eq_u32_e32 vcc, 0, v2
	s_and_saveexec_b64 s[16:17], vcc
	s_cbranch_execz .LBB0_1358
	s_bcnt1_i32_b64 s0, s[14:15]
	v_mov_b32_e32 v3, 0x3000
	v_mov_b32_e32 v4, s0
	global_atomic_add v3, v3, v4, s[10:11] offset:1024 sc0

.LBB0_1372:
	s_or_b64 exec, exec, s[10:11]
	s_mov_b64 s[10:11], exec
	v_mbcnt_lo_u32_b32 v1, s10, 0
	v_mbcnt_hi_u32_b32 v1, s11, v1
	v_cmp_eq_u32_e32 vcc, 0, v1
	s_waitcnt vmcnt(0)
	s_and_saveexec_b64 s[14:15], vcc
	s_cbranch_execz .LBB0_1374
	s_bcnt1_i32_b64 s0, s[10:11]
	v_mov_b32_e32 v1, 0x2000
	v_mov_b32_e32 v2, s0
	global_atomic_add v1, v2, s[12:13] offset:1024

.LBB0_1576:
	s_or_b64 exec, exec, s[18:19]
	v_cvt_f32_u32_e32 v5, v3
	s_waitcnt vmcnt(0)
	v_readfirstlane_b32 s16, v4
	v_sub_u32_e32 v4, 0, v3
	v_rcp_iflag_f32_e32 v5, v5
	v_add_u32_e32 v6, s16, v2
	v_mul_f32_e32 v5, 0x4f7ffffe, v5
	v_cvt_u32_f32_e32 v5, v5
	v_mul_lo_u32 v2, v4, v5
	v_mul_hi_u32 v2, v5, v2
	v_add_u32_e32 v2, v5, v2
	v_mul_hi_u32 v2, v6, v2
	v_mul_lo_u32 v4, v2, v3
	v_sub_u32_e32 v4, v6, v4
	v_add_u32_e32 v5, 1, v2
	v_cmp_ge_u32_e32 vcc, v4, v3
	s_nop 1
	v_cndmask_b32_e32 v2, v2, v5, vcc
	v_sub_u32_e32 v5, v4, v3
	v_cndmask_b32_e32 v4, v4, v5, vcc
	v_add_u32_e32 v5, 1, v2
	v_cmp_ge_u32_e32 vcc, v4, v3
	v_add_u32_e32 v4, 1, v6
	s_nop 0
	v_cndmask_b32_e32 v2, v2, v5, vcc
	v_mul_lo_u32 v5, v3, v2
	v_add_u32_e32 v3, v5, v3
	v_cmp_ne_u32_e32 vcc, v4, v3
	s_and_saveexec_b64 s[16:17], vcc
	s_xor_b64 s[16:17], exec, s[16:17]
	s_cbranch_execz .LBB0_1590
	buffer_inv sc1
	s_waitcnt lgkmcnt(0)
	v_mov_b32_e32 v1, 0x2000
	global_load_dword v1, v1, s[14:15] offset:1024 sc1
	s_add_u32 s22, s14, 0x2400
	s_addc_u32 s23, s15, 0
	s_waitcnt vmcnt(0)
	v_cmp_eq_u32_e32 vcc, v1, v2
	s_and_saveexec_b64 s[18:19], vcc
	s_cbranch_execz .LBB0_1589
	s_mov_b32 s33, 1
	s_mov_b64 s[24:25], 0
	v_mov_b32_e32 v1, 0
	s_branch .LBB0_1580

.LBB0_1589:
	s_or_b64 exec, exec, s[18:19]
	s_waitcnt vmcnt(0)
	s_waitcnt vmcnt(0)
.LBB0_1590:
	s_andn2_saveexec_b64 s[16:17], s[16:17]
	s_cbranch_execz .LBB0_1610
	s_mov_b64 s[16:17], exec
	buffer_wbl2 sc1
	buffer_inv sc1
	s_waitcnt lgkmcnt(0)
	s_waitcnt vmcnt(0)
	v_mbcnt_lo_u32_b32 v2, s16, 0
	v_mbcnt_hi_u32_b32 v2, s17, v2
	v_cmp_eq_u32_e32 vcc, 0, v2
	s_and_saveexec_b64 s[18:19], vcc
	s_cbranch_execz .LBB0_1593
	s_bcnt1_i32_b64 s16, s[16:17]
	v_mov_b32_e32 v3, 0x3000
	v_mov_b32_e32 v4, s16
	global_atomic_add v3, v3, v4, s[12:13] offset:1024 sc0

.LBB0_1607:
	s_or_b64 exec, exec, s[12:13]
	s_mov_b64 s[12:13], exec
	v_mbcnt_lo_u32_b32 v1, s12, 0
	v_mbcnt_hi_u32_b32 v1, s13, v1
	v_cmp_eq_u32_e32 vcc, 0, v1
	s_waitcnt vmcnt(0)
	s_and_saveexec_b64 s[16:17], vcc
	s_cbranch_execz .LBB0_1609
	s_bcnt1_i32_b64 s12, s[12:13]
	v_mov_b32_e32 v1, 0x2000
	v_mov_b32_e32 v2, s12
	global_atomic_add v1, v2, s[14:15] offset:1024

.LBB0_1698:
	s_or_b64 exec, exec, s[12:13]
	v_cvt_f32_u32_e32 v5, v3
	s_waitcnt vmcnt(0)
	v_readfirstlane_b32 s0, v4
	v_sub_u32_e32 v4, 0, v3
	v_rcp_iflag_f32_e32 v5, v5
	v_add_u32_e32 v6, s0, v2
	v_mul_f32_e32 v5, 0x4f7ffffe, v5
	v_cvt_u32_f32_e32 v5, v5
	v_mul_lo_u32 v2, v4, v5
	v_mul_hi_u32 v2, v5, v2
	v_add_u32_e32 v2, v5, v2
	v_mul_hi_u32 v2, v6, v2
	v_mul_lo_u32 v4, v2, v3
	v_sub_u32_e32 v4, v6, v4
	v_add_u32_e32 v5, 1, v2
	v_cmp_ge_u32_e32 vcc, v4, v3
	s_nop 1
	v_cndmask_b32_e32 v2, v2, v5, vcc
	v_sub_u32_e32 v5, v4, v3
	v_cndmask_b32_e32 v4, v4, v5, vcc
	v_add_u32_e32 v5, 1, v2
	v_cmp_ge_u32_e32 vcc, v4, v3
	v_add_u32_e32 v4, 1, v6
	s_nop 0
	v_cndmask_b32_e32 v2, v2, v5, vcc
	v_mul_lo_u32 v5, v3, v2
	v_add_u32_e32 v3, v5, v3
	v_cmp_ne_u32_e32 vcc, v4, v3
	s_and_saveexec_b64 s[0:1], vcc
	s_xor_b64 s[10:11], exec, s[0:1]
	s_cbranch_execz .LBB0_1712
	buffer_inv sc1
	s_waitcnt lgkmcnt(0)
	v_mov_b32_e32 v1, 0x2000
	global_load_dword v1, v1, s[8:9] offset:1024 sc1
	s_add_u32 s14, s8, 0x2400
	s_addc_u32 s15, s9, 0
	s_waitcnt vmcnt(0)
	v_cmp_eq_u32_e32 vcc, v1, v2
	s_and_saveexec_b64 s[12:13], vcc
	s_cbranch_execz .LBB0_1711
	s_mov_b32 s0, 1
	s_mov_b64 s[16:17], 0
	v_mov_b32_e32 v1, 0
	s_branch .LBB0_1702

.LBB0_1711:
	s_or_b64 exec, exec, s[12:13]
	s_waitcnt vmcnt(0)
	s_waitcnt vmcnt(0)
.LBB0_1712:
	s_andn2_saveexec_b64 s[0:1], s[10:11]
	s_cbranch_execz .LBB0_1732
	s_mov_b64 s[10:11], exec
	buffer_wbl2 sc1
	buffer_inv sc1
	s_waitcnt lgkmcnt(0)
	s_waitcnt vmcnt(0)
	v_mbcnt_lo_u32_b32 v2, s10, 0
	v_mbcnt_hi_u32_b32 v2, s11, v2
	v_cmp_eq_u32_e32 vcc, 0, v2
	s_and_saveexec_b64 s[12:13], vcc
	s_cbranch_execz .LBB0_1715
	s_bcnt1_i32_b64 s0, s[10:11]
	v_mov_b32_e32 v3, 0x3000
	v_mov_b32_e32 v4, s0
	global_atomic_add v3, v3, v4, s[4:5] offset:1024 sc0

.LBB0_1729:
	s_or_b64 exec, exec, s[4:5]
	s_mov_b64 s[4:5], exec
	v_mbcnt_lo_u32_b32 v1, s4, 0
	v_mbcnt_hi_u32_b32 v1, s5, v1
	v_cmp_eq_u32_e32 vcc, 0, v1
	s_waitcnt vmcnt(0)
	s_and_saveexec_b64 s[10:11], vcc
	s_cbranch_execz .LBB0_1731
	s_bcnt1_i32_b64 s0, s[4:5]
	v_mov_b32_e32 v1, 0x2000
	v_mov_b32_e32 v2, s0
	global_atomic_add v1, v2, s[8:9] offset:1024
